# adaLN GEMV: the bias element of the reduce stage is requested before the K loop instead of after the partial-sum barrier
# speedup vs baseline: 1.0057x; 1.0057x over previous
.LBB0_11:
	s_mul_hi_i32 s10, s14, 0x2aaaaaab
	s_lshr_b32 s11, s10, 31
	s_ashr_i32 s15, s10, 4
	s_add_i32 s15, s15, s11
	s_mul_i32 s10, s15, 0x60
	s_sub_i32 s10, s14, s10
	s_lshl_b32 s10, s10, 6
	s_ashr_i32 s11, s10, 31
	s_mul_i32 s17, s15, 0x1800000
	s_lshl_b64 s[12:13], s[10:11], 2
	s_mul_hi_i32 s16, s15, 0x1800000
	s_add_u32 s12, s17, s12
	s_addc_u32 s13, s16, s13
	v_lshl_add_u64 v[36:37], v[34:35], 0, s[12:13]
	s_movk_i32 s12, 0xffe0
	s_mul_i32 s12, s15, 0x1800
	s_add_i32 s12, s12, s10
	v_readlane_b32 s56, v249, 10
	v_readlane_b32 s57, v249, 11
	v_or_b32_e32 v138, s12, v30
	v_lshlrev_b32_e32 v138, 2, v138
	v_add_co_u32_e32 v136, vcc, 0xfff46000, v36
	s_mov_b64 s[16:17], 0x6000
	v_addc_co_u32_e32 v137, vcc, -1, v37, vcc
	v_mov_b32_e32 v38, 0
	v_mov_b32_e32 v39, v33
	ds_read_b128 v[104:107], v27
	ds_read_b128 v[108:111], v27 offset:16
	ds_read_b128 v[112:115], v27 offset:4096
	ds_read_b128 v[116:119], v27 offset:4112
	s_nop 1
	global_load_dword v139, v138, s[56:57]
	global_load_dword v40, v[136:137], off nt
	v_lshl_add_u64 v[136:137], v[136:137], 0, s[16:17]
	global_load_dword v41, v[136:137], off nt
	v_lshl_add_u64 v[136:137], v[136:137], 0, s[16:17]
	global_load_dword v42, v[136:137], off nt
	v_lshl_add_u64 v[136:137], v[136:137], 0, s[16:17]
	global_load_dword v43, v[136:137], off nt
	v_lshl_add_u64 v[136:137], v[136:137], 0, s[16:17]
	global_load_dword v44, v[136:137], off nt
	v_lshl_add_u64 v[136:137], v[136:137], 0, s[16:17]
	global_load_dword v45, v[136:137], off nt
	v_lshl_add_u64 v[136:137], v[136:137], 0, s[16:17]
	global_load_dword v46, v[136:137], off nt
	v_lshl_add_u64 v[136:137], v[136:137], 0, s[16:17]
	global_load_dword v47, v[136:137], off nt
	v_lshl_add_u64 v[136:137], v[136:137], 0, s[16:17]
	global_load_dword v48, v[136:137], off nt
	v_lshl_add_u64 v[136:137], v[136:137], 0, s[16:17]
	global_load_dword v49, v[136:137], off nt
	v_lshl_add_u64 v[136:137], v[136:137], 0, s[16:17]
	global_load_dword v50, v[136:137], off nt
	v_lshl_add_u64 v[136:137], v[136:137], 0, s[16:17]
	global_load_dword v51, v[136:137], off nt
	v_lshl_add_u64 v[136:137], v[136:137], 0, s[16:17]
	global_load_dword v52, v[136:137], off nt
	v_lshl_add_u64 v[136:137], v[136:137], 0, s[16:17]
	global_load_dword v53, v[136:137], off nt
	v_lshl_add_u64 v[136:137], v[136:137], 0, s[16:17]
	global_load_dword v54, v[136:137], off nt
	v_lshl_add_u64 v[136:137], v[136:137], 0, s[16:17]
	global_load_dword v55, v[136:137], off nt
	v_lshl_add_u64 v[136:137], v[136:137], 0, s[16:17]
	global_load_dword v56, v[136:137], off nt
	v_lshl_add_u64 v[136:137], v[136:137], 0, s[16:17]
	global_load_dword v57, v[136:137], off nt
	v_lshl_add_u64 v[136:137], v[136:137], 0, s[16:17]
	global_load_dword v58, v[136:137], off nt
	v_lshl_add_u64 v[136:137], v[136:137], 0, s[16:17]
	global_load_dword v59, v[136:137], off nt
	v_lshl_add_u64 v[136:137], v[136:137], 0, s[16:17]
	global_load_dword v60, v[136:137], off nt
	v_lshl_add_u64 v[136:137], v[136:137], 0, s[16:17]
	global_load_dword v61, v[136:137], off nt
	v_lshl_add_u64 v[136:137], v[136:137], 0, s[16:17]
	global_load_dword v62, v[136:137], off nt
	v_lshl_add_u64 v[136:137], v[136:137], 0, s[16:17]
	global_load_dword v63, v[136:137], off nt
	v_lshl_add_u64 v[136:137], v[136:137], 0, s[16:17]
	global_load_dword v64, v[136:137], off nt
	v_lshl_add_u64 v[136:137], v[136:137], 0, s[16:17]
	global_load_dword v65, v[136:137], off nt
	v_lshl_add_u64 v[136:137], v[136:137], 0, s[16:17]
	global_load_dword v66, v[136:137], off nt
	v_lshl_add_u64 v[136:137], v[136:137], 0, s[16:17]
	global_load_dword v67, v[136:137], off nt
	v_lshl_add_u64 v[136:137], v[136:137], 0, s[16:17]
	global_load_dword v68, v[136:137], off nt
	v_lshl_add_u64 v[136:137], v[136:137], 0, s[16:17]
	global_load_dword v69, v[136:137], off nt
	v_lshl_add_u64 v[136:137], v[136:137], 0, s[16:17]
	global_load_dword v70, v[136:137], off nt
	v_lshl_add_u64 v[136:137], v[136:137], 0, s[16:17]
	global_load_dword v71, v[136:137], off nt
	v_lshl_add_u64 v[136:137], v[136:137], 0, s[16:17]
	global_load_dword v72, v[136:137], off nt
	v_lshl_add_u64 v[136:137], v[136:137], 0, s[16:17]
	global_load_dword v73, v[136:137], off nt
	v_lshl_add_u64 v[136:137], v[136:137], 0, s[16:17]
	global_load_dword v74, v[136:137], off nt
	v_lshl_add_u64 v[136:137], v[136:137], 0, s[16:17]
	global_load_dword v75, v[136:137], off nt
	v_lshl_add_u64 v[136:137], v[136:137], 0, s[16:17]
	global_load_dword v76, v[136:137], off nt
	v_lshl_add_u64 v[136:137], v[136:137], 0, s[16:17]
	global_load_dword v77, v[136:137], off nt
	v_lshl_add_u64 v[136:137], v[136:137], 0, s[16:17]
	global_load_dword v78, v[136:137], off nt
	v_lshl_add_u64 v[136:137], v[136:137], 0, s[16:17]
	global_load_dword v79, v[136:137], off nt
	v_lshl_add_u64 v[136:137], v[136:137], 0, s[16:17]
	global_load_dword v80, v[136:137], off nt
	v_lshl_add_u64 v[136:137], v[136:137], 0, s[16:17]
	global_load_dword v81, v[136:137], off nt
	v_lshl_add_u64 v[136:137], v[136:137], 0, s[16:17]
	global_load_dword v82, v[136:137], off nt
	v_lshl_add_u64 v[136:137], v[136:137], 0, s[16:17]
	global_load_dword v83, v[136:137], off nt
	v_lshl_add_u64 v[136:137], v[136:137], 0, s[16:17]
	global_load_dword v84, v[136:137], off nt
	v_lshl_add_u64 v[136:137], v[136:137], 0, s[16:17]
	global_load_dword v85, v[136:137], off nt
	v_lshl_add_u64 v[136:137], v[136:137], 0, s[16:17]
	global_load_dword v86, v[136:137], off nt
	v_lshl_add_u64 v[136:137], v[136:137], 0, s[16:17]
	global_load_dword v87, v[136:137], off nt
	v_lshl_add_u64 v[136:137], v[136:137], 0, s[16:17]
	ds_read_b128 v[120:123], v27 offset:32
	ds_read_b128 v[124:127], v27 offset:48
	ds_read_b128 v[128:131], v27 offset:4128
	ds_read_b128 v[132:135], v27 offset:4144
	s_waitcnt lgkmcnt(4)
	s_waitcnt vmcnt(47)
	v_fma_f32 v38, v40, v104, v38
	v_fma_f32 v39, v40, v112, v39
	global_load_dword v40, v[136:137], off nt
	v_lshl_add_u64 v[136:137], v[136:137], 0, s[16:17]
	s_waitcnt vmcnt(47)
	v_fma_f32 v38, v41, v105, v38
	v_fma_f32 v39, v41, v113, v39
	global_load_dword v41, v[136:137], off nt
	v_lshl_add_u64 v[136:137], v[136:137], 0, s[16:17]
	s_waitcnt vmcnt(47)
	v_fma_f32 v38, v42, v106, v38
	v_fma_f32 v39, v42, v114, v39
	global_load_dword v42, v[136:137], off nt
	v_lshl_add_u64 v[136:137], v[136:137], 0, s[16:17]
	s_waitcnt vmcnt(47)
	v_fma_f32 v38, v43, v107, v38
	v_fma_f32 v39, v43, v115, v39
	global_load_dword v43, v[136:137], off nt
	v_lshl_add_u64 v[136:137], v[136:137], 0, s[16:17]
	s_waitcnt vmcnt(47)
	v_fma_f32 v38, v44, v108, v38
	v_fma_f32 v39, v44, v116, v39
	global_load_dword v44, v[136:137], off nt
	v_lshl_add_u64 v[136:137], v[136:137], 0, s[16:17]
	s_waitcnt vmcnt(47)
	v_fma_f32 v38, v45, v109, v38
	v_fma_f32 v39, v45, v117, v39
	global_load_dword v45, v[136:137], off nt
	v_lshl_add_u64 v[136:137], v[136:137], 0, s[16:17]
	s_waitcnt vmcnt(47)
	v_fma_f32 v38, v46, v110, v38
	v_fma_f32 v39, v46, v118, v39
	global_load_dword v46, v[136:137], off nt
	v_lshl_add_u64 v[136:137], v[136:137], 0, s[16:17]
	s_waitcnt vmcnt(47)
	v_fma_f32 v38, v47, v111, v38
	v_fma_f32 v39, v47, v119, v39
	global_load_dword v47, v[136:137], off nt
	v_lshl_add_u64 v[136:137], v[136:137], 0, s[16:17]
	ds_read_b128 v[104:107], v27 offset:64
	ds_read_b128 v[108:111], v27 offset:80
	ds_read_b128 v[112:115], v27 offset:4160
	ds_read_b128 v[116:119], v27 offset:4176
	s_waitcnt lgkmcnt(4)
	s_waitcnt vmcnt(47)
	v_fma_f32 v38, v48, v120, v38
	v_fma_f32 v39, v48, v128, v39
	global_load_dword v48, v[136:137], off nt
	v_lshl_add_u64 v[136:137], v[136:137], 0, s[16:17]
	s_waitcnt vmcnt(47)
	v_fma_f32 v38, v49, v121, v38
	v_fma_f32 v39, v49, v129, v39
	global_load_dword v49, v[136:137], off nt
	v_lshl_add_u64 v[136:137], v[136:137], 0, s[16:17]
	s_waitcnt vmcnt(47)
	v_fma_f32 v38, v50, v122, v38
	v_fma_f32 v39, v50, v130, v39
	global_load_dword v50, v[136:137], off nt
	v_lshl_add_u64 v[136:137], v[136:137], 0, s[16:17]
	s_waitcnt vmcnt(47)
	v_fma_f32 v38, v51, v123, v38
	v_fma_f32 v39, v51, v131, v39
	global_load_dword v51, v[136:137], off nt
	v_lshl_add_u64 v[136:137], v[136:137], 0, s[16:17]
	s_waitcnt vmcnt(47)
	v_fma_f32 v38, v52, v124, v38
	v_fma_f32 v39, v52, v132, v39
	global_load_dword v52, v[136:137], off nt
	v_lshl_add_u64 v[136:137], v[136:137], 0, s[16:17]
	s_waitcnt vmcnt(47)
	v_fma_f32 v38, v53, v125, v38
	v_fma_f32 v39, v53, v133, v39
	global_load_dword v53, v[136:137], off nt
	v_lshl_add_u64 v[136:137], v[136:137], 0, s[16:17]
	s_waitcnt vmcnt(47)
	v_fma_f32 v38, v54, v126, v38
	v_fma_f32 v39, v54, v134, v39
	global_load_dword v54, v[136:137], off nt
	v_lshl_add_u64 v[136:137], v[136:137], 0, s[16:17]
	s_waitcnt vmcnt(47)
	v_fma_f32 v38, v55, v127, v38
	v_fma_f32 v39, v55, v135, v39
	global_load_dword v55, v[136:137], off nt
	v_lshl_add_u64 v[136:137], v[136:137], 0, s[16:17]
	ds_read_b128 v[120:123], v27 offset:96
	ds_read_b128 v[124:127], v27 offset:112
	ds_read_b128 v[128:131], v27 offset:4192
	ds_read_b128 v[132:135], v27 offset:4208
	s_waitcnt lgkmcnt(4)
	s_waitcnt vmcnt(47)
	v_fma_f32 v38, v56, v104, v38
	v_fma_f32 v39, v56, v112, v39
	global_load_dword v56, v[136:137], off nt
	v_lshl_add_u64 v[136:137], v[136:137], 0, s[16:17]
	s_waitcnt vmcnt(47)
	v_fma_f32 v38, v57, v105, v38
	v_fma_f32 v39, v57, v113, v39
	global_load_dword v57, v[136:137], off nt
	v_lshl_add_u64 v[136:137], v[136:137], 0, s[16:17]
	s_waitcnt vmcnt(47)
	v_fma_f32 v38, v58, v106, v38
	v_fma_f32 v39, v58, v114, v39
	global_load_dword v58, v[136:137], off nt
	v_lshl_add_u64 v[136:137], v[136:137], 0, s[16:17]
	s_waitcnt vmcnt(47)
	v_fma_f32 v38, v59, v107, v38
	v_fma_f32 v39, v59, v115, v39
	global_load_dword v59, v[136:137], off nt
	v_lshl_add_u64 v[136:137], v[136:137], 0, s[16:17]
	s_waitcnt vmcnt(47)
	v_fma_f32 v38, v60, v108, v38
	v_fma_f32 v39, v60, v116, v39
	global_load_dword v60, v[136:137], off nt
	v_lshl_add_u64 v[136:137], v[136:137], 0, s[16:17]
	s_waitcnt vmcnt(47)
	v_fma_f32 v38, v61, v109, v38
	v_fma_f32 v39, v61, v117, v39
	global_load_dword v61, v[136:137], off nt
	v_lshl_add_u64 v[136:137], v[136:137], 0, s[16:17]
	s_waitcnt vmcnt(47)
	v_fma_f32 v38, v62, v110, v38
	v_fma_f32 v39, v62, v118, v39
	global_load_dword v62, v[136:137], off nt
	v_lshl_add_u64 v[136:137], v[136:137], 0, s[16:17]
	s_waitcnt vmcnt(47)
	v_fma_f32 v38, v63, v111, v38
	v_fma_f32 v39, v63, v119, v39
	global_load_dword v63, v[136:137], off nt
	v_lshl_add_u64 v[136:137], v[136:137], 0, s[16:17]
	ds_read_b128 v[104:107], v27 offset:128
	ds_read_b128 v[108:111], v27 offset:144
	ds_read_b128 v[112:115], v27 offset:4224
	ds_read_b128 v[116:119], v27 offset:4240
	s_waitcnt lgkmcnt(4)
	s_waitcnt vmcnt(47)
	v_fma_f32 v38, v64, v120, v38
	v_fma_f32 v39, v64, v128, v39
	global_load_dword v64, v[136:137], off nt
	v_lshl_add_u64 v[136:137], v[136:137], 0, s[16:17]
	s_waitcnt vmcnt(47)
	v_fma_f32 v38, v65, v121, v38
	v_fma_f32 v39, v65, v129, v39
	global_load_dword v65, v[136:137], off nt
	v_lshl_add_u64 v[136:137], v[136:137], 0, s[16:17]
	s_waitcnt vmcnt(47)
	v_fma_f32 v38, v66, v122, v38
	v_fma_f32 v39, v66, v130, v39
	global_load_dword v66, v[136:137], off nt
	v_lshl_add_u64 v[136:137], v[136:137], 0, s[16:17]
	s_waitcnt vmcnt(47)
	v_fma_f32 v38, v67, v123, v38
	v_fma_f32 v39, v67, v131, v39
	global_load_dword v67, v[136:137], off nt
	v_lshl_add_u64 v[136:137], v[136:137], 0, s[16:17]
	s_waitcnt vmcnt(47)
	v_fma_f32 v38, v68, v124, v38
	v_fma_f32 v39, v68, v132, v39
	global_load_dword v68, v[136:137], off nt
	v_lshl_add_u64 v[136:137], v[136:137], 0, s[16:17]
	s_waitcnt vmcnt(47)
	v_fma_f32 v38, v69, v125, v38
	v_fma_f32 v39, v69, v133, v39
	global_load_dword v69, v[136:137], off nt
	v_lshl_add_u64 v[136:137], v[136:137], 0, s[16:17]
	s_waitcnt vmcnt(47)
	v_fma_f32 v38, v70, v126, v38
	v_fma_f32 v39, v70, v134, v39
	global_load_dword v70, v[136:137], off nt
	v_lshl_add_u64 v[136:137], v[136:137], 0, s[16:17]
	s_waitcnt vmcnt(47)
	v_fma_f32 v38, v71, v127, v38
	v_fma_f32 v39, v71, v135, v39
	global_load_dword v71, v[136:137], off nt
	v_lshl_add_u64 v[136:137], v[136:137], 0, s[16:17]
	ds_read_b128 v[120:123], v27 offset:160
	ds_read_b128 v[124:127], v27 offset:176
	ds_read_b128 v[128:131], v27 offset:4256
	ds_read_b128 v[132:135], v27 offset:4272
	s_waitcnt lgkmcnt(4)
	s_waitcnt vmcnt(47)
	v_fma_f32 v38, v72, v104, v38
	v_fma_f32 v39, v72, v112, v39
	global_load_dword v72, v[136:137], off nt
	v_lshl_add_u64 v[136:137], v[136:137], 0, s[16:17]
	s_waitcnt vmcnt(47)
	v_fma_f32 v38, v73, v105, v38
	v_fma_f32 v39, v73, v113, v39
	global_load_dword v73, v[136:137], off nt
	v_lshl_add_u64 v[136:137], v[136:137], 0, s[16:17]
	s_waitcnt vmcnt(47)
	v_fma_f32 v38, v74, v106, v38
	v_fma_f32 v39, v74, v114, v39
	global_load_dword v74, v[136:137], off nt
	v_lshl_add_u64 v[136:137], v[136:137], 0, s[16:17]
	s_waitcnt vmcnt(47)
	v_fma_f32 v38, v75, v107, v38
	v_fma_f32 v39, v75, v115, v39
	global_load_dword v75, v[136:137], off nt
	v_lshl_add_u64 v[136:137], v[136:137], 0, s[16:17]
	s_waitcnt vmcnt(47)
	v_fma_f32 v38, v76, v108, v38
	v_fma_f32 v39, v76, v116, v39
	global_load_dword v76, v[136:137], off nt
	v_lshl_add_u64 v[136:137], v[136:137], 0, s[16:17]
	s_waitcnt vmcnt(47)
	v_fma_f32 v38, v77, v109, v38
	v_fma_f32 v39, v77, v117, v39
	global_load_dword v77, v[136:137], off nt
	v_lshl_add_u64 v[136:137], v[136:137], 0, s[16:17]
	s_waitcnt vmcnt(47)
	v_fma_f32 v38, v78, v110, v38
	v_fma_f32 v39, v78, v118, v39
	global_load_dword v78, v[136:137], off nt
	v_lshl_add_u64 v[136:137], v[136:137], 0, s[16:17]
	s_waitcnt vmcnt(47)
	v_fma_f32 v38, v79, v111, v38
	v_fma_f32 v39, v79, v119, v39
	global_load_dword v79, v[136:137], off nt
	v_lshl_add_u64 v[136:137], v[136:137], 0, s[16:17]
	ds_read_b128 v[104:107], v27 offset:192
	ds_read_b128 v[108:111], v27 offset:208
	ds_read_b128 v[112:115], v27 offset:4288
	ds_read_b128 v[116:119], v27 offset:4304
	s_waitcnt lgkmcnt(4)
	s_waitcnt vmcnt(47)
	v_fma_f32 v38, v80, v120, v38
	v_fma_f32 v39, v80, v128, v39
	global_load_dword v80, v[136:137], off nt
	v_lshl_add_u64 v[136:137], v[136:137], 0, s[16:17]
	s_waitcnt vmcnt(47)
	v_fma_f32 v38, v81, v121, v38
	v_fma_f32 v39, v81, v129, v39
	global_load_dword v81, v[136:137], off nt
	v_lshl_add_u64 v[136:137], v[136:137], 0, s[16:17]
	s_waitcnt vmcnt(47)
	v_fma_f32 v38, v82, v122, v38
	v_fma_f32 v39, v82, v130, v39
	global_load_dword v82, v[136:137], off nt
	v_lshl_add_u64 v[136:137], v[136:137], 0, s[16:17]
	s_waitcnt vmcnt(47)
	v_fma_f32 v38, v83, v123, v38
	v_fma_f32 v39, v83, v131, v39
	global_load_dword v83, v[136:137], off nt
	v_lshl_add_u64 v[136:137], v[136:137], 0, s[16:17]
	s_waitcnt vmcnt(47)
	v_fma_f32 v38, v84, v124, v38
	v_fma_f32 v39, v84, v132, v39
	global_load_dword v84, v[136:137], off nt
	v_lshl_add_u64 v[136:137], v[136:137], 0, s[16:17]
	s_waitcnt vmcnt(47)
	v_fma_f32 v38, v85, v125, v38
	v_fma_f32 v39, v85, v133, v39
	global_load_dword v85, v[136:137], off nt
	v_lshl_add_u64 v[136:137], v[136:137], 0, s[16:17]
	s_waitcnt vmcnt(47)
	v_fma_f32 v38, v86, v126, v38
	v_fma_f32 v39, v86, v134, v39
	global_load_dword v86, v[136:137], off nt
	v_lshl_add_u64 v[136:137], v[136:137], 0, s[16:17]
	s_waitcnt vmcnt(47)
	v_fma_f32 v38, v87, v127, v38
	v_fma_f32 v39, v87, v135, v39
	global_load_dword v87, v[136:137], off nt
	v_lshl_add_u64 v[136:137], v[136:137], 0, s[16:17]
	ds_read_b128 v[120:123], v27 offset:224
	ds_read_b128 v[124:127], v27 offset:240
	ds_read_b128 v[128:131], v27 offset:4320
	ds_read_b128 v[132:135], v27 offset:4336
	s_waitcnt lgkmcnt(4)
	s_waitcnt vmcnt(47)
	v_fma_f32 v38, v40, v104, v38
	v_fma_f32 v39, v40, v112, v39
	global_load_dword v40, v[136:137], off nt
	v_lshl_add_u64 v[136:137], v[136:137], 0, s[16:17]
	s_waitcnt vmcnt(47)
	v_fma_f32 v38, v41, v105, v38
	v_fma_f32 v39, v41, v113, v39
	global_load_dword v41, v[136:137], off nt
	v_lshl_add_u64 v[136:137], v[136:137], 0, s[16:17]
	s_waitcnt vmcnt(47)
	v_fma_f32 v38, v42, v106, v38
	v_fma_f32 v39, v42, v114, v39
	global_load_dword v42, v[136:137], off nt
	v_lshl_add_u64 v[136:137], v[136:137], 0, s[16:17]
	s_waitcnt vmcnt(47)
	v_fma_f32 v38, v43, v107, v38
	v_fma_f32 v39, v43, v115, v39
	global_load_dword v43, v[136:137], off nt
	v_lshl_add_u64 v[136:137], v[136:137], 0, s[16:17]
	s_waitcnt vmcnt(47)
	v_fma_f32 v38, v44, v108, v38
	v_fma_f32 v39, v44, v116, v39
	global_load_dword v44, v[136:137], off nt
	v_lshl_add_u64 v[136:137], v[136:137], 0, s[16:17]
	s_waitcnt vmcnt(47)
	v_fma_f32 v38, v45, v109, v38
	v_fma_f32 v39, v45, v117, v39
	global_load_dword v45, v[136:137], off nt
	v_lshl_add_u64 v[136:137], v[136:137], 0, s[16:17]
	s_waitcnt vmcnt(47)
	v_fma_f32 v38, v46, v110, v38
	v_fma_f32 v39, v46, v118, v39
	global_load_dword v46, v[136:137], off nt
	v_lshl_add_u64 v[136:137], v[136:137], 0, s[16:17]
	s_waitcnt vmcnt(47)
	v_fma_f32 v38, v47, v111, v38
	v_fma_f32 v39, v47, v119, v39
	global_load_dword v47, v[136:137], off nt
	v_lshl_add_u64 v[136:137], v[136:137], 0, s[16:17]
	ds_read_b128 v[104:107], v27 offset:256
	ds_read_b128 v[108:111], v27 offset:272
	ds_read_b128 v[112:115], v27 offset:4352
	ds_read_b128 v[116:119], v27 offset:4368
	s_waitcnt lgkmcnt(4)
	s_waitcnt vmcnt(47)
	v_fma_f32 v38, v48, v120, v38
	v_fma_f32 v39, v48, v128, v39
	global_load_dword v48, v[136:137], off nt
	v_lshl_add_u64 v[136:137], v[136:137], 0, s[16:17]
	s_waitcnt vmcnt(47)
	v_fma_f32 v38, v49, v121, v38
	v_fma_f32 v39, v49, v129, v39
	global_load_dword v49, v[136:137], off nt
	v_lshl_add_u64 v[136:137], v[136:137], 0, s[16:17]
	s_waitcnt vmcnt(47)
	v_fma_f32 v38, v50, v122, v38
	v_fma_f32 v39, v50, v130, v39
	global_load_dword v50, v[136:137], off nt
	v_lshl_add_u64 v[136:137], v[136:137], 0, s[16:17]
	s_waitcnt vmcnt(47)
	v_fma_f32 v38, v51, v123, v38
	v_fma_f32 v39, v51, v131, v39
	global_load_dword v51, v[136:137], off nt
	v_lshl_add_u64 v[136:137], v[136:137], 0, s[16:17]
	s_waitcnt vmcnt(47)
	v_fma_f32 v38, v52, v124, v38
	v_fma_f32 v39, v52, v132, v39
	global_load_dword v52, v[136:137], off nt
	v_lshl_add_u64 v[136:137], v[136:137], 0, s[16:17]
	s_waitcnt vmcnt(47)
	v_fma_f32 v38, v53, v125, v38
	v_fma_f32 v39, v53, v133, v39
	global_load_dword v53, v[136:137], off nt
	v_lshl_add_u64 v[136:137], v[136:137], 0, s[16:17]
	s_waitcnt vmcnt(47)
	v_fma_f32 v38, v54, v126, v38
	v_fma_f32 v39, v54, v134, v39
	global_load_dword v54, v[136:137], off nt
	v_lshl_add_u64 v[136:137], v[136:137], 0, s[16:17]
	s_waitcnt vmcnt(47)
	v_fma_f32 v38, v55, v127, v38
	v_fma_f32 v39, v55, v135, v39
	global_load_dword v55, v[136:137], off nt
	v_lshl_add_u64 v[136:137], v[136:137], 0, s[16:17]
	ds_read_b128 v[120:123], v27 offset:288
	ds_read_b128 v[124:127], v27 offset:304
	ds_read_b128 v[128:131], v27 offset:4384
	ds_read_b128 v[132:135], v27 offset:4400
	s_waitcnt lgkmcnt(4)
	s_waitcnt vmcnt(47)
	v_fma_f32 v38, v56, v104, v38
	v_fma_f32 v39, v56, v112, v39
	global_load_dword v56, v[136:137], off nt
	v_lshl_add_u64 v[136:137], v[136:137], 0, s[16:17]
	s_waitcnt vmcnt(47)
	v_fma_f32 v38, v57, v105, v38
	v_fma_f32 v39, v57, v113, v39
	global_load_dword v57, v[136:137], off nt
	v_lshl_add_u64 v[136:137], v[136:137], 0, s[16:17]
	s_waitcnt vmcnt(47)
	v_fma_f32 v38, v58, v106, v38
	v_fma_f32 v39, v58, v114, v39
	global_load_dword v58, v[136:137], off nt
	v_lshl_add_u64 v[136:137], v[136:137], 0, s[16:17]
	s_waitcnt vmcnt(47)
	v_fma_f32 v38, v59, v107, v38
	v_fma_f32 v39, v59, v115, v39
	global_load_dword v59, v[136:137], off nt
	v_lshl_add_u64 v[136:137], v[136:137], 0, s[16:17]
	s_waitcnt vmcnt(47)
	v_fma_f32 v38, v60, v108, v38
	v_fma_f32 v39, v60, v116, v39
	global_load_dword v60, v[136:137], off nt
	v_lshl_add_u64 v[136:137], v[136:137], 0, s[16:17]
	s_waitcnt vmcnt(47)
	v_fma_f32 v38, v61, v109, v38
	v_fma_f32 v39, v61, v117, v39
	global_load_dword v61, v[136:137], off nt
	v_lshl_add_u64 v[136:137], v[136:137], 0, s[16:17]
	s_waitcnt vmcnt(47)
	v_fma_f32 v38, v62, v110, v38
	v_fma_f32 v39, v62, v118, v39
	global_load_dword v62, v[136:137], off nt
	v_lshl_add_u64 v[136:137], v[136:137], 0, s[16:17]
	s_waitcnt vmcnt(47)
	v_fma_f32 v38, v63, v111, v38
	v_fma_f32 v39, v63, v119, v39
	global_load_dword v63, v[136:137], off nt
	v_lshl_add_u64 v[136:137], v[136:137], 0, s[16:17]
	ds_read_b128 v[104:107], v27 offset:320
	ds_read_b128 v[108:111], v27 offset:336
	ds_read_b128 v[112:115], v27 offset:4416
	ds_read_b128 v[116:119], v27 offset:4432
	s_waitcnt lgkmcnt(4)
	s_waitcnt vmcnt(47)
	v_fma_f32 v38, v64, v120, v38
	v_fma_f32 v39, v64, v128, v39
	global_load_dword v64, v[136:137], off nt
	v_lshl_add_u64 v[136:137], v[136:137], 0, s[16:17]
	s_waitcnt vmcnt(47)
	v_fma_f32 v38, v65, v121, v38
	v_fma_f32 v39, v65, v129, v39
	global_load_dword v65, v[136:137], off nt
	v_lshl_add_u64 v[136:137], v[136:137], 0, s[16:17]
	s_waitcnt vmcnt(47)
	v_fma_f32 v38, v66, v122, v38
	v_fma_f32 v39, v66, v130, v39
	global_load_dword v66, v[136:137], off nt
	v_lshl_add_u64 v[136:137], v[136:137], 0, s[16:17]
	s_waitcnt vmcnt(47)
	v_fma_f32 v38, v67, v123, v38
	v_fma_f32 v39, v67, v131, v39
	global_load_dword v67, v[136:137], off nt
	v_lshl_add_u64 v[136:137], v[136:137], 0, s[16:17]
	s_waitcnt vmcnt(47)
	v_fma_f32 v38, v68, v124, v38
	v_fma_f32 v39, v68, v132, v39
	global_load_dword v68, v[136:137], off nt
	v_lshl_add_u64 v[136:137], v[136:137], 0, s[16:17]
	s_waitcnt vmcnt(47)
	v_fma_f32 v38, v69, v125, v38
	v_fma_f32 v39, v69, v133, v39
	global_load_dword v69, v[136:137], off nt
	v_lshl_add_u64 v[136:137], v[136:137], 0, s[16:17]
	s_waitcnt vmcnt(47)
	v_fma_f32 v38, v70, v126, v38
	v_fma_f32 v39, v70, v134, v39
	global_load_dword v70, v[136:137], off nt
	v_lshl_add_u64 v[136:137], v[136:137], 0, s[16:17]
	s_waitcnt vmcnt(47)
	v_fma_f32 v38, v71, v127, v38
	v_fma_f32 v39, v71, v135, v39
	global_load_dword v71, v[136:137], off nt
	ds_read_b128 v[120:123], v27 offset:352
	ds_read_b128 v[124:127], v27 offset:368
	ds_read_b128 v[128:131], v27 offset:4448
	ds_read_b128 v[132:135], v27 offset:4464
	s_waitcnt lgkmcnt(4)
	s_waitcnt vmcnt(47)
	v_fma_f32 v38, v72, v104, v38
	v_fma_f32 v39, v72, v112, v39
	s_waitcnt vmcnt(46)
	v_fma_f32 v38, v73, v105, v38
	v_fma_f32 v39, v73, v113, v39
	s_waitcnt vmcnt(45)
	v_fma_f32 v38, v74, v106, v38
	v_fma_f32 v39, v74, v114, v39
	s_waitcnt vmcnt(44)
	v_fma_f32 v38, v75, v107, v38
	v_fma_f32 v39, v75, v115, v39
	s_waitcnt vmcnt(43)
	v_fma_f32 v38, v76, v108, v38
	v_fma_f32 v39, v76, v116, v39
	s_waitcnt vmcnt(42)
	v_fma_f32 v38, v77, v109, v38
	v_fma_f32 v39, v77, v117, v39
	s_waitcnt vmcnt(41)
	v_fma_f32 v38, v78, v110, v38
	v_fma_f32 v39, v78, v118, v39
	s_waitcnt vmcnt(40)
	v_fma_f32 v38, v79, v111, v38
	v_fma_f32 v39, v79, v119, v39
	ds_read_b128 v[104:107], v27 offset:384
	ds_read_b128 v[108:111], v27 offset:400
	ds_read_b128 v[112:115], v27 offset:4480
	ds_read_b128 v[116:119], v27 offset:4496
	s_waitcnt lgkmcnt(4)
	s_waitcnt vmcnt(39)
	v_fma_f32 v38, v80, v120, v38
	v_fma_f32 v39, v80, v128, v39
	s_waitcnt vmcnt(38)
	v_fma_f32 v38, v81, v121, v38
	v_fma_f32 v39, v81, v129, v39
	s_waitcnt vmcnt(37)
	v_fma_f32 v38, v82, v122, v38
	v_fma_f32 v39, v82, v130, v39
	s_waitcnt vmcnt(36)
	v_fma_f32 v38, v83, v123, v38
	v_fma_f32 v39, v83, v131, v39
	s_waitcnt vmcnt(35)
	v_fma_f32 v38, v84, v124, v38
	v_fma_f32 v39, v84, v132, v39
	s_waitcnt vmcnt(34)
	v_fma_f32 v38, v85, v125, v38
	v_fma_f32 v39, v85, v133, v39
	s_waitcnt vmcnt(33)
	v_fma_f32 v38, v86, v126, v38
	v_fma_f32 v39, v86, v134, v39
	s_waitcnt vmcnt(32)
	v_fma_f32 v38, v87, v127, v38
	v_fma_f32 v39, v87, v135, v39
	ds_read_b128 v[120:123], v27 offset:416
	ds_read_b128 v[124:127], v27 offset:432
	ds_read_b128 v[128:131], v27 offset:4512
	ds_read_b128 v[132:135], v27 offset:4528
	s_waitcnt lgkmcnt(4)
	s_waitcnt vmcnt(31)
	v_fma_f32 v38, v40, v104, v38
	v_fma_f32 v39, v40, v112, v39
	s_waitcnt vmcnt(30)
	v_fma_f32 v38, v41, v105, v38
	v_fma_f32 v39, v41, v113, v39
	s_waitcnt vmcnt(29)
	v_fma_f32 v38, v42, v106, v38
	v_fma_f32 v39, v42, v114, v39
	s_waitcnt vmcnt(28)
	v_fma_f32 v38, v43, v107, v38
	v_fma_f32 v39, v43, v115, v39
	s_waitcnt vmcnt(27)
	v_fma_f32 v38, v44, v108, v38
	v_fma_f32 v39, v44, v116, v39
	s_waitcnt vmcnt(26)
	v_fma_f32 v38, v45, v109, v38
	v_fma_f32 v39, v45, v117, v39
	s_waitcnt vmcnt(25)
	v_fma_f32 v38, v46, v110, v38
	v_fma_f32 v39, v46, v118, v39
	s_waitcnt vmcnt(24)
	v_fma_f32 v38, v47, v111, v38
	v_fma_f32 v39, v47, v119, v39
	ds_read_b128 v[104:107], v27 offset:448
	ds_read_b128 v[108:111], v27 offset:464
	ds_read_b128 v[112:115], v27 offset:4544
	ds_read_b128 v[116:119], v27 offset:4560
	s_waitcnt lgkmcnt(4)
	s_waitcnt vmcnt(23)
	v_fma_f32 v38, v48, v120, v38
	v_fma_f32 v39, v48, v128, v39
	s_waitcnt vmcnt(22)
	v_fma_f32 v38, v49, v121, v38
	v_fma_f32 v39, v49, v129, v39
	s_waitcnt vmcnt(21)
	v_fma_f32 v38, v50, v122, v38
	v_fma_f32 v39, v50, v130, v39
	s_waitcnt vmcnt(20)
	v_fma_f32 v38, v51, v123, v38
	v_fma_f32 v39, v51, v131, v39
	s_waitcnt vmcnt(19)
	v_fma_f32 v38, v52, v124, v38
	v_fma_f32 v39, v52, v132, v39
	s_waitcnt vmcnt(18)
	v_fma_f32 v38, v53, v125, v38
	v_fma_f32 v39, v53, v133, v39
	s_waitcnt vmcnt(17)
	v_fma_f32 v38, v54, v126, v38
	v_fma_f32 v39, v54, v134, v39
	s_waitcnt vmcnt(16)
	v_fma_f32 v38, v55, v127, v38
	v_fma_f32 v39, v55, v135, v39
	ds_read_b128 v[120:123], v27 offset:480
	ds_read_b128 v[124:127], v27 offset:496
	ds_read_b128 v[128:131], v27 offset:4576
	ds_read_b128 v[132:135], v27 offset:4592
	s_waitcnt lgkmcnt(4)
	s_waitcnt vmcnt(15)
	v_fma_f32 v38, v56, v104, v38
	v_fma_f32 v39, v56, v112, v39
	s_waitcnt vmcnt(14)
	v_fma_f32 v38, v57, v105, v38
	v_fma_f32 v39, v57, v113, v39
	s_waitcnt vmcnt(13)
	v_fma_f32 v38, v58, v106, v38
	v_fma_f32 v39, v58, v114, v39
	s_waitcnt vmcnt(12)
	v_fma_f32 v38, v59, v107, v38
	v_fma_f32 v39, v59, v115, v39
	s_waitcnt vmcnt(11)
	v_fma_f32 v38, v60, v108, v38
	v_fma_f32 v39, v60, v116, v39
	s_waitcnt vmcnt(10)
	v_fma_f32 v38, v61, v109, v38
	v_fma_f32 v39, v61, v117, v39
	s_waitcnt vmcnt(9)
	v_fma_f32 v38, v62, v110, v38
	v_fma_f32 v39, v62, v118, v39
	s_waitcnt vmcnt(8)
	v_fma_f32 v38, v63, v111, v38
	v_fma_f32 v39, v63, v119, v39
	s_waitcnt lgkmcnt(0)
	s_waitcnt vmcnt(7)
	v_fma_f32 v38, v64, v120, v38
	v_fma_f32 v39, v64, v128, v39
	s_waitcnt vmcnt(6)
	v_fma_f32 v38, v65, v121, v38
	v_fma_f32 v39, v65, v129, v39
	s_waitcnt vmcnt(5)
	v_fma_f32 v38, v66, v122, v38
	v_fma_f32 v39, v66, v130, v39
	s_waitcnt vmcnt(4)
	v_fma_f32 v38, v67, v123, v38
	v_fma_f32 v39, v67, v131, v39
	s_waitcnt vmcnt(3)
	v_fma_f32 v38, v68, v124, v38
	v_fma_f32 v39, v68, v132, v39
	s_waitcnt vmcnt(2)
	v_fma_f32 v38, v69, v125, v38
	v_fma_f32 v39, v69, v133, v39
	s_waitcnt vmcnt(1)
	v_fma_f32 v38, v70, v126, v38
	v_fma_f32 v39, v70, v134, v39
	s_waitcnt vmcnt(0)
	v_fma_f32 v38, v71, v127, v38
	v_fma_f32 v39, v71, v135, v39
	ds_write2st64_b32 v29, v38, v39 offset0:32 offset1:33
	s_waitcnt lgkmcnt(0)
	s_barrier
	s_and_saveexec_b64 s[12:13], s[0:1]
	s_cbranch_execz .LBB0_15
	s_mul_i32 s16, s15, 0x1800
	s_add_i32 s16, s16, s10
	v_or_b32_e32 v0, s16, v30
	v_readlane_b32 s48, v249, 2
	v_ashrrev_i32_e32 v1, 31, v0
	v_readlane_b32 s56, v249, 10
	v_readlane_b32 s57, v249, 11
	v_readlane_b32 s49, v249, 3
	v_readlane_b32 s50, v249, 4
	v_lshl_add_u64 v[0:1], v[0:1], 2, s[56:57]
	v_mov_b32_e32 v6, v139
	ds_read2st64_b32 v[0:1], v31 offset0:32 offset1:34
	ds_read2st64_b32 v[2:3], v31 offset0:36 offset1:38
	ds_read2st64_b32 v[4:5], v31 offset0:40 offset1:42
	v_readlane_b32 s51, v249, 5
	v_readlane_b32 s52, v249, 6
	s_waitcnt lgkmcnt(2)
	v_add_f32_e32 v0, 0, v0
	v_add_f32_e32 v7, v0, v1
	ds_read2st64_b32 v[0:1], v31 offset0:44 offset1:46
	s_waitcnt lgkmcnt(2)
	v_add_f32_e32 v2, v7, v2
	v_add_f32_e32 v2, v2, v3
	s_waitcnt lgkmcnt(1)
	v_add_f32_e32 v2, v2, v4
	v_add_f32_e32 v2, v2, v5
	s_waitcnt lgkmcnt(0)
	v_add_f32_e32 v0, v2, v0
	v_add_f32_e32 v2, v0, v1
	v_lshl_add_u32 v3, s15, 1, v23
	v_mov_b64_e32 v[0:1], s[96:97]
	v_mad_i64_i32 v[0:1], s[16:17], v3, s3, v[0:1]
	v_lshl_add_u64 v[0:1], s[10:11], 2, v[0:1]
	v_lshl_add_u64 v[0:1], v[0:1], 0, v[32:33]
	v_readlane_b32 s53, v249, 7
	v_readlane_b32 s54, v249, 8
	v_readlane_b32 s55, v249, 9
	v_readlane_b32 s58, v249, 12
	v_readlane_b32 s59, v249, 13
	v_readlane_b32 s60, v249, 14
	v_readlane_b32 s61, v249, 15
	v_readlane_b32 s62, v249, 16
	v_readlane_b32 s63, v249, 17
	s_waitcnt vmcnt(0)
	v_add_f32_e32 v2, v2, v6
	global_store_dword v[0:1], v2, off sc1
